# first-unit scheduler of both MoE phases reads the expert counters from the LDS copy (was 4 chained L2 round trips per phase start)
# baseline (speedup 1.0000x reference)
.LBB0_915:
	v_mov_b32_e32 v6, v0
	s_cmp_ge_i32 s90, s14
	v_readfirstlane_b32 s4, v6
	s_cbranch_scc1 .LBB0_934
	v_mov_b32_e32 v163, 0
	v_mov_b32_e32 v182, 0x20800
	ds_read_b128 v[8:11], v182
	ds_read_b128 v[12:15], v182 offset:16
	ds_read_b128 v[2:5], v182 offset:48
	ds_read_b128 v[16:19], v182 offset:32
	s_ashr_i32 s1, s90, 31
	s_lshr_b32 s2, s1, 29
	s_add_i32 s2, s90, s2
	s_ashr_i32 s3, s2, 3
	s_and_b32 s2, s2, -8
	s_sub_i32 s2, s90, s2
	v_mov_b32_e32 v1, s2
	v_alignbit_b32 v1, s0, v1, 31
	s_ashr_i32 s5, s4, 6
	v_readfirstlane_b32 s6, v1
	s_mul_i32 s2, s6, s2
	s_add_i32 s2, s2, s3
	s_ashr_i32 s3, s2, 31
	s_lshr_b32 s3, s3, 26
	s_add_i32 s6, s2, s3
	s_ashr_i32 s3, s6, 6
	s_lshl_b32 s7, s3, 2
	s_sub_i32 s3, s0, s7
	s_min_i32 s8, s3, 4
	s_abs_i32 s9, s8
	v_cvt_f32_u32_e32 v1, s9
	s_sub_i32 s11, 0, s9
	s_andn2_b32 s6, s6, 63
	s_sub_i32 s2, s2, s6
	v_rcp_iflag_f32_e32 v1, v1
	s_abs_i32 s6, s2
	s_xor_b32 s10, s2, s8
	s_ashr_i32 s28, s4, 8
	v_mul_f32_e32 v1, 0x4f7ffffe, v1
	v_cvt_u32_f32_e32 v1, v1
	s_lshl_b32 s3, s5, 10
	s_ashr_i32 s10, s10, 31
	v_mov_b32_e32 v165, v163
	v_readfirstlane_b32 s12, v1
	s_mul_i32 s11, s11, s12
	s_mul_hi_u32 s11, s12, s11
	s_add_i32 s12, s12, s11
	s_mul_hi_u32 s11, s6, s12
	s_mul_i32 s12, s11, s9
	s_sub_i32 s6, s6, s12
	s_add_i32 s13, s11, 1
	s_sub_i32 s12, s6, s9
	s_cmp_ge_u32 s6, s9
	s_cselect_b32 s11, s13, s11
	s_cselect_b32 s6, s12, s6
	s_add_i32 s12, s11, 1
	s_cmp_ge_u32 s6, s9
	s_cselect_b32 s6, s12, s11
	s_xor_b32 s6, s6, s10
	s_sub_i32 s40, s6, s10
	s_mul_i32 s6, s40, s8
	s_sub_i32 s2, s2, s6
	s_add_i32 s2, s2, s7
	s_cmp_gt_i32 s2, -1
	s_cselect_b64 s[8:9], -1, 0
	s_mov_b32 s59, 0
	v_mov_b32_e32 v171, v163
	v_mov_b32_e32 v173, v163
	s_waitcnt lgkmcnt(3)
	v_add_u32_e32 v1, 0xff, v8
	v_ashrrev_i32_e32 v1, 8, v1
	v_add_u32_e32 v7, 0xff, v9
	v_cmp_lt_i32_e32 vcc, s2, v1
	v_add_u32_e32 v8, 0xff, v10
	v_ashrrev_i32_e32 v7, 8, v7
	s_and_b64 s[10:11], s[8:9], vcc
	v_add_u32_e32 v9, 0xff, v11
	v_ashrrev_i32_e32 v8, 8, v8
	v_add_u32_e32 v7, v7, v1
	s_and_b64 s[10:11], s[10:11], exec
	v_ashrrev_i32_e32 v9, 8, v9
	v_cmp_ge_i32_e64 s[6:7], s2, v1
	v_cmp_lt_i32_e32 vcc, s2, v7
	v_add_u32_e32 v8, v8, v7
	s_cselect_b32 s22, s2, 0
	v_sub_u32_e32 v1, s2, v1
	v_cmp_ge_i32_e64 s[8:9], s2, v7
	v_cmp_lt_i32_e64 s[10:11], s2, v8
	v_add_u32_e32 v9, v9, v8
	s_and_b64 vcc, s[6:7], vcc
	v_mov_b32_e32 v11, s22
	v_sub_u32_e32 v7, s2, v7
	v_cmp_ge_i32_e64 s[12:13], s2, v8
	v_cmp_lt_i32_e64 s[6:7], s2, v9
	s_and_b64 s[8:9], s[8:9], s[10:11]
	v_cndmask_b32_e32 v1, v11, v1, vcc
	v_sub_u32_e32 v8, s2, v8
	v_cndmask_b32_e64 v10, 0, 1, vcc
	v_cndmask_b32_e64 v1, v1, v7, s[8:9]
	s_and_b64 vcc, s[12:13], s[6:7]
	v_cndmask_b32_e32 v1, v1, v8, vcc
	s_waitcnt lgkmcnt(2)
	v_add_u32_e32 v8, 0xff, v12
	v_ashrrev_i32_e32 v8, 8, v8
	v_cndmask_b32_e64 v10, v10, 2, s[8:9]
	v_add_u32_e32 v8, v8, v9
	v_cndmask_b32_e64 v7, v10, 3, vcc
	v_cmp_ge_i32_e32 vcc, s2, v9
	v_cmp_lt_i32_e64 s[6:7], s2, v8
	v_sub_u32_e32 v9, s2, v9
	s_and_b64 vcc, vcc, s[6:7]
	v_cndmask_b32_e32 v1, v1, v9, vcc
	v_add_u32_e32 v9, 0xff, v13
	v_ashrrev_i32_e32 v9, 8, v9
	v_add_u32_e32 v9, v9, v8
	v_cndmask_b32_e64 v7, v7, 4, vcc
	v_cmp_ge_i32_e32 vcc, s2, v8
	v_cmp_lt_i32_e64 s[6:7], s2, v9
	v_sub_u32_e32 v8, s2, v8
	s_and_b64 vcc, vcc, s[6:7]
	v_cndmask_b32_e32 v1, v1, v8, vcc
	v_add_u32_e32 v8, 0xff, v14
	v_ashrrev_i32_e32 v8, 8, v8
	v_add_u32_e32 v20, v8, v9
	v_cndmask_b32_e64 v7, v7, 5, vcc
	v_cmp_ge_i32_e32 vcc, s2, v9
	v_cmp_lt_i32_e64 s[6:7], s2, v20
	v_sub_u32_e32 v8, s2, v9
	s_and_b64 vcc, vcc, s[6:7]
	v_cndmask_b32_e32 v1, v1, v8, vcc
	v_add_u32_e32 v8, 0xff, v15
	v_ashrrev_i32_e32 v8, 8, v8
	v_add_u32_e32 v21, v8, v20
	ds_read_b128 v[8:11], v182 offset:80
	ds_read_b128 v[12:15], v182 offset:64
	s_waitcnt lgkmcnt(2)
	v_add_u32_e32 v16, 0xff, v16
	v_cndmask_b32_e64 v7, v7, 6, vcc
	v_cmp_ge_i32_e32 vcc, s2, v20
	v_cmp_lt_i32_e64 s[6:7], s2, v21
	v_ashrrev_i32_e32 v16, 8, v16
	v_sub_u32_e32 v20, s2, v20
	s_and_b64 vcc, vcc, s[6:7]
	v_add_u32_e32 v16, v16, v21
	v_add_u32_e32 v17, 0xff, v17
	v_cndmask_b32_e64 v7, v7, 7, vcc
	v_cndmask_b32_e32 v1, v1, v20, vcc
	v_cmp_ge_i32_e32 vcc, s2, v21
	v_cmp_lt_i32_e64 s[6:7], s2, v16
	v_ashrrev_i32_e32 v17, 8, v17
	v_sub_u32_e32 v20, s2, v21
	s_and_b64 vcc, vcc, s[6:7]
	v_add_u32_e32 v17, v17, v16
	v_cndmask_b32_e64 v7, v7, 8, vcc
	v_cndmask_b32_e32 v1, v1, v20, vcc
	v_cmp_ge_i32_e32 vcc, s2, v16
	v_cmp_lt_i32_e64 s[6:7], s2, v17
	v_sub_u32_e32 v16, s2, v16
	s_and_b64 vcc, vcc, s[6:7]
	v_cndmask_b32_e32 v1, v1, v16, vcc
	v_add_u32_e32 v16, 0xff, v18
	v_ashrrev_i32_e32 v16, 8, v16
	v_add_u32_e32 v16, v16, v17
	v_cndmask_b32_e64 v7, v7, 9, vcc
	v_cmp_ge_i32_e32 vcc, s2, v17
	v_cmp_lt_i32_e64 s[6:7], s2, v16
	v_sub_u32_e32 v17, s2, v17
	s_and_b64 vcc, vcc, s[6:7]
	v_cndmask_b32_e32 v1, v1, v17, vcc
	v_add_u32_e32 v17, 0xff, v19
	v_ashrrev_i32_e32 v17, 8, v17
	v_add_u32_e32 v17, v17, v16
	v_add_u32_e32 v2, 0xff, v2
	v_cndmask_b32_e64 v7, v7, 10, vcc
	v_cmp_ge_i32_e32 vcc, s2, v16
	v_cmp_lt_i32_e64 s[6:7], s2, v17
	v_ashrrev_i32_e32 v2, 8, v2
	v_sub_u32_e32 v16, s2, v16
	s_and_b64 vcc, vcc, s[6:7]
	v_add_u32_e32 v2, v2, v17
	v_add_u32_e32 v3, 0xff, v3
	v_cndmask_b32_e64 v7, v7, 11, vcc
	v_cndmask_b32_e32 v1, v1, v16, vcc
	v_cmp_ge_i32_e32 vcc, s2, v17
	v_cmp_lt_i32_e64 s[6:7], s2, v2
	v_ashrrev_i32_e32 v3, 8, v3
	v_sub_u32_e32 v16, s2, v17
	s_and_b64 vcc, vcc, s[6:7]
	v_add_u32_e32 v3, v3, v2
	v_cndmask_b32_e64 v7, v7, 12, vcc
	v_cndmask_b32_e32 v1, v1, v16, vcc
	v_cmp_ge_i32_e32 vcc, s2, v2
	v_cmp_lt_i32_e64 s[6:7], s2, v3
	v_sub_u32_e32 v2, s2, v2
	s_and_b64 vcc, vcc, s[6:7]
	v_cndmask_b32_e32 v1, v1, v2, vcc
	v_add_u32_e32 v2, 0xff, v4
	v_ashrrev_i32_e32 v2, 8, v2
	v_add_u32_e32 v20, v2, v3
	v_cndmask_b32_e64 v7, v7, 13, vcc
	v_cmp_ge_i32_e32 vcc, s2, v3
	v_cmp_lt_i32_e64 s[6:7], s2, v20
	v_sub_u32_e32 v2, s2, v3
	s_and_b64 vcc, vcc, s[6:7]
	v_cndmask_b32_e32 v1, v1, v2, vcc
	v_add_u32_e32 v2, 0xff, v5
	v_ashrrev_i32_e32 v21, 8, v2
	ds_read_b128 v[2:5], v182 offset:112
	ds_read_b128 v[16:19], v182 offset:96
	v_add_u32_e32 v21, v21, v20
	v_cndmask_b32_e64 v7, v7, 14, vcc
	v_cmp_ge_i32_e32 vcc, s2, v20
	v_cmp_lt_i32_e64 s[6:7], s2, v21
	v_sub_u32_e32 v20, s2, v20
	s_and_b64 vcc, vcc, s[6:7]
	v_cndmask_b32_e64 v7, v7, 15, vcc
	s_waitcnt lgkmcnt(2)
	v_add_u32_e32 v12, 0xff, v12
	v_ashrrev_i32_e32 v12, 8, v12
	v_add_u32_e32 v12, v12, v21
	v_add_u32_e32 v13, 0xff, v13
	v_cndmask_b32_e32 v1, v1, v20, vcc
	v_cmp_ge_i32_e32 vcc, s2, v21
	v_cmp_lt_i32_e64 s[6:7], s2, v12
	v_ashrrev_i32_e32 v13, 8, v13
	v_sub_u32_e32 v20, s2, v21
	s_and_b64 vcc, vcc, s[6:7]
	v_add_u32_e32 v13, v13, v12
	v_cndmask_b32_e64 v7, v7, 16, vcc
	v_cndmask_b32_e32 v1, v1, v20, vcc
	v_cmp_ge_i32_e32 vcc, s2, v12
	v_cmp_lt_i32_e64 s[6:7], s2, v13
	v_sub_u32_e32 v12, s2, v12
	s_and_b64 vcc, vcc, s[6:7]
	v_cndmask_b32_e32 v1, v1, v12, vcc
	v_add_u32_e32 v12, 0xff, v14
	v_ashrrev_i32_e32 v12, 8, v12
	v_add_u32_e32 v12, v12, v13
	v_cndmask_b32_e64 v7, v7, 17, vcc
	v_cmp_ge_i32_e32 vcc, s2, v13
	v_cmp_lt_i32_e64 s[6:7], s2, v12
	v_sub_u32_e32 v13, s2, v13
	s_and_b64 vcc, vcc, s[6:7]
	v_cndmask_b32_e32 v1, v1, v13, vcc
	v_add_u32_e32 v13, 0xff, v15
	v_ashrrev_i32_e32 v13, 8, v13
	v_add_u32_e32 v13, v13, v12
	v_add_u32_e32 v8, 0xff, v8
	v_cndmask_b32_e64 v7, v7, 18, vcc
	v_cmp_ge_i32_e32 vcc, s2, v12
	v_cmp_lt_i32_e64 s[6:7], s2, v13
	v_ashrrev_i32_e32 v8, 8, v8
	v_sub_u32_e32 v12, s2, v12
	s_and_b64 vcc, vcc, s[6:7]
	v_add_u32_e32 v8, v8, v13
	v_add_u32_e32 v9, 0xff, v9
	v_cndmask_b32_e64 v7, v7, 19, vcc
	v_cndmask_b32_e32 v1, v1, v12, vcc
	v_cmp_ge_i32_e32 vcc, s2, v13
	v_cmp_lt_i32_e64 s[6:7], s2, v8
	v_ashrrev_i32_e32 v9, 8, v9
	v_sub_u32_e32 v12, s2, v13
	s_and_b64 vcc, vcc, s[6:7]
	v_add_u32_e32 v9, v9, v8
	v_cndmask_b32_e64 v7, v7, 20, vcc
	v_cndmask_b32_e32 v1, v1, v12, vcc
	v_cmp_ge_i32_e32 vcc, s2, v8
	v_cmp_lt_i32_e64 s[6:7], s2, v9
	v_sub_u32_e32 v8, s2, v8
	s_and_b64 vcc, vcc, s[6:7]
	v_cndmask_b32_e32 v1, v1, v8, vcc
	v_add_u32_e32 v8, 0xff, v10
	v_ashrrev_i32_e32 v8, 8, v8
	v_add_u32_e32 v8, v8, v9
	v_cndmask_b32_e64 v7, v7, 21, vcc
	v_cmp_ge_i32_e32 vcc, s2, v9
	v_cmp_lt_i32_e64 s[6:7], s2, v8
	v_sub_u32_e32 v9, s2, v9
	s_and_b64 vcc, vcc, s[6:7]
	v_cndmask_b32_e32 v1, v1, v9, vcc
	v_add_u32_e32 v9, 0xff, v11
	v_ashrrev_i32_e32 v9, 8, v9
	v_add_u32_e32 v9, v9, v8
	v_cndmask_b32_e64 v7, v7, 22, vcc
	v_cmp_ge_i32_e32 vcc, s2, v8
	v_cmp_lt_i32_e64 s[6:7], s2, v9
	v_sub_u32_e32 v8, s2, v8
	s_and_b64 vcc, vcc, s[6:7]
	v_cndmask_b32_e32 v1, v1, v8, vcc
	s_waitcnt lgkmcnt(0)
	v_add_u32_e32 v8, 0xff, v16
	v_ashrrev_i32_e32 v8, 8, v8
	v_add_u32_e32 v8, v8, v9
	v_cndmask_b32_e64 v7, v7, 23, vcc
	v_cmp_ge_i32_e32 vcc, s2, v9
	v_cmp_lt_i32_e64 s[6:7], s2, v8
	v_sub_u32_e32 v9, s2, v9
	s_and_b64 vcc, vcc, s[6:7]
	v_cndmask_b32_e32 v1, v1, v9, vcc
	v_add_u32_e32 v9, 0xff, v17
	v_ashrrev_i32_e32 v9, 8, v9
	v_add_u32_e32 v9, v9, v8
	v_cndmask_b32_e64 v7, v7, 24, vcc
	v_cmp_ge_i32_e32 vcc, s2, v8
	v_cmp_lt_i32_e64 s[6:7], s2, v9
	v_sub_u32_e32 v8, s2, v8
	s_and_b64 vcc, vcc, s[6:7]
	v_cndmask_b32_e32 v1, v1, v8, vcc
	v_add_u32_e32 v8, 0xff, v18
	v_ashrrev_i32_e32 v8, 8, v8
	v_add_u32_e32 v8, v8, v9
	v_cndmask_b32_e64 v7, v7, 25, vcc
	v_cmp_ge_i32_e32 vcc, s2, v9
	v_cmp_lt_i32_e64 s[6:7], s2, v8
	v_sub_u32_e32 v9, s2, v9
	s_and_b64 vcc, vcc, s[6:7]
	v_cndmask_b32_e32 v1, v1, v9, vcc
	v_add_u32_e32 v9, 0xff, v19
	v_ashrrev_i32_e32 v9, 8, v9
	v_add_u32_e32 v9, v9, v8
	v_add_u32_e32 v2, 0xff, v2
	v_cndmask_b32_e64 v7, v7, 26, vcc
	v_cmp_ge_i32_e32 vcc, s2, v8
	v_cmp_lt_i32_e64 s[6:7], s2, v9
	v_ashrrev_i32_e32 v2, 8, v2
	v_sub_u32_e32 v8, s2, v8
	s_and_b64 vcc, vcc, s[6:7]
	v_add_u32_e32 v2, v2, v9
	v_add_u32_e32 v3, 0xff, v3
	v_cndmask_b32_e64 v7, v7, 27, vcc
	v_cndmask_b32_e32 v1, v1, v8, vcc
	v_cmp_ge_i32_e32 vcc, s2, v9
	v_cmp_lt_i32_e64 s[6:7], s2, v2
	v_ashrrev_i32_e32 v3, 8, v3
	v_sub_u32_e32 v8, s2, v9
	s_and_b64 vcc, vcc, s[6:7]
	v_add_u32_e32 v3, v3, v2
	v_cndmask_b32_e64 v7, v7, 28, vcc
	v_cndmask_b32_e32 v1, v1, v8, vcc
	v_cmp_ge_i32_e32 vcc, s2, v2
	v_cmp_lt_i32_e64 s[6:7], s2, v3
	v_sub_u32_e32 v2, s2, v2
	s_and_b64 vcc, vcc, s[6:7]
	v_cndmask_b32_e32 v1, v1, v2, vcc
	v_add_u32_e32 v2, 0xff, v4
	v_ashrrev_i32_e32 v2, 8, v2
	v_add_u32_e32 v2, v2, v3
	v_cndmask_b32_e64 v7, v7, 29, vcc
	v_cmp_ge_i32_e32 vcc, s2, v3
	v_cmp_lt_i32_e64 s[6:7], s2, v2
	v_sub_u32_e32 v3, s2, v3
	s_and_b64 vcc, vcc, s[6:7]
	v_cndmask_b32_e32 v1, v1, v3, vcc
	v_add_u32_e32 v3, 0xff, v5
	v_ashrrev_i32_e32 v3, 8, v3
	v_add_u32_e32 v3, v3, v2
	v_cndmask_b32_e64 v4, v7, 30, vcc
	v_cmp_ge_i32_e32 vcc, s2, v2
	v_cmp_lt_i32_e64 s[6:7], s2, v3
	v_sub_u32_e32 v2, s2, v2
	s_and_b64 vcc, vcc, s[6:7]
	v_cndmask_b32_e32 v1, v1, v2, vcc
	v_cndmask_b32_e64 v3, v4, 31, vcc
	v_readfirstlane_b32 s6, v1
	s_lshl_b32 s10, s6, 8
	v_readfirstlane_b32 s42, v3
	s_add_u32 s37, s18, 0x5e000000
	s_addc_u32 s50, s19, 0
	s_ashr_i32 s43, s42, 31
	s_ashr_i32 s41, s40, 31
	s_lshl_b64 s[6:7], s[40:41], 19
	s_lshl_b64 s[8:9], s[42:43], 23
	s_add_u32 s8, s37, s8
	s_addc_u32 s9, s50, s9
	s_add_u32 s44, s8, s6
	s_addc_u32 s45, s9, s7
	s_add_u32 s41, s18, 0x800000
	s_addc_u32 s51, s19, 0
	s_lshl_b64 s[6:7], s[42:43], 2
	s_add_u32 s6, s18, s6
	v_mov_b32_e32 v1, v0
	s_addc_u32 s7, s19, s7
	global_load_dword v2, v163, s[6:7]
	v_lshlrev_b32_e32 v11, 4, v1
	v_ashrrev_i32_e32 v3, 31, v6
	v_lshrrev_b32_e32 v3, 26, v3
	v_add_u32_e32 v3, v6, v3
	v_ashrrev_i32_e32 v8, 6, v3
	v_bfe_i32 v3, v6, 27, 1
	v_lshlrev_b32_e32 v7, 4, v6
	v_lshrrev_b32_e32 v3, 22, v3
	v_add_u32_e32 v3, v7, v3
	v_and_b32_e32 v3, 0xfffffc00, v3
	v_sub_u32_e32 v9, v7, v3
	v_lshrrev_b32_e32 v10, 4, v9
	s_waitcnt vmcnt(0)
	v_readfirstlane_b32 s6, v2
	v_ashrrev_i32_e32 v2, 31, v1
	v_lshrrev_b32_e32 v2, 26, v2
	v_add_u32_e32 v2, v1, v2
	v_bfe_i32 v1, v1, 27, 1
	v_lshrrev_b32_e32 v1, 22, v1
	v_add_u32_e32 v1, v11, v1
	v_and_b32_e32 v1, 0xfffffc00, v1
	v_sub_u32_e32 v1, v11, v1
	v_ashrrev_i32_e32 v12, 6, v2
	v_lshrrev_b32_e32 v2, 4, v1
	v_bitop3_b32 v13, v2, v1, 32 bitop3:0x6c
	v_ashrrev_i32_e32 v1, 31, v1
	v_lshrrev_b32_e32 v1, 26, v1
	v_lshlrev_b32_e32 v2, 3, v12
	v_add_u32_e32 v1, v13, v1
	s_add_i32 s8, s6, -1
	v_and_b32_e32 v2, -16, v2
	v_ashrrev_i32_e32 v14, 6, v1
	s_lshl_b64 s[6:7], s[42:43], 16
	v_add_u32_e32 v1, v14, v2
	s_add_u32 s6, s41, s6
	v_add_u32_e32 v2, s10, v1
	s_addc_u32 s7, s51, s7
	s_or_b32 s9, s10, 0x80
	v_min_i32_e32 v2, s8, v2
	v_add_u32_e32 v1, s9, v1
	v_ashrrev_i32_e32 v3, 31, v2
	v_min_i32_e32 v4, s8, v1
	v_lshl_add_u64 v[2:3], v[2:3], 2, s[6:7]
	v_ashrrev_i32_e32 v5, 31, v4
	v_add_u32_e32 v1, 0x2000, v11
	v_lshl_add_u64 v[4:5], v[4:5], 2, s[6:7]
	global_load_dword v15, v[2:3], off
	global_load_dword v16, v[4:5], off
	v_ashrrev_i32_e32 v2, 31, v1
	v_lshrrev_b32_e32 v2, 22, v2
	v_add_u32_e32 v2, v1, v2
	v_ashrrev_i32_e32 v4, 10, v2
	v_mul_i32_i24_e32 v2, 0x400, v4
	v_sub_u32_e32 v1, v1, v2
	v_lshrrev_b32_e32 v2, 4, v1
	v_bitop3_b32 v5, v2, v1, 32 bitop3:0x6c
	v_ashrrev_i32_e32 v2, 31, v5
	v_lshrrev_b32_e32 v2, 26, v2
	v_lshlrev_b32_e32 v1, 3, v4
	v_add_u32_e32 v11, v5, v2
	v_and_b32_e32 v1, -16, v1
	v_ashrrev_i32_e32 v2, 6, v11
	v_add_u32_e32 v1, v2, v1
	v_add_u32_e32 v2, s10, v1
	v_min_i32_e32 v2, s8, v2
	v_ashrrev_i32_e32 v3, 31, v2
	v_lshl_add_u64 v[2:3], v[2:3], 2, s[6:7]
	v_add_u32_e32 v1, s9, v1
	global_load_dword v17, v[2:3], off
	v_min_i32_e32 v2, s8, v1
	v_ashrrev_i32_e32 v3, 31, v2
	v_lshl_add_u64 v[2:3], v[2:3], 2, s[6:7]
	global_load_dword v2, v[2:3], off
	v_bitop3_b32 v1, v10, v9, 32 bitop3:0x6c
	v_ashrrev_i32_e32 v9, 31, v9
	v_lshrrev_b32_e32 v9, 26, v9
	v_add_u32_e32 v9, v1, v9
	v_lshlrev_b32_e32 v3, 3, v8
	v_ashrrev_i32_e32 v9, 6, v9
	v_and_b32_e32 v3, -16, v3
	v_mul_i32_i24_e32 v10, 64, v9
	v_add_u32_e32 v3, v9, v3
	v_sub_u32_e32 v10, v1, v10
	v_mov_b32_e32 v1, 1
	v_lshlrev_b32_e32 v8, 5, v8
	v_ashrrev_i16_sdwa v10, v1, sext(v10) dst_sel:DWORD dst_unused:UNUSED_PAD src0_sel:DWORD src1_sel:BYTE_0
	v_lshlrev_b32_e32 v18, 1, v3
	v_lshrrev_b32_e32 v19, 2, v3
	v_and_b32_e32 v9, 3, v9
	s_mov_b32 s6, 0x1fffe0
	v_and_b32_e32 v8, 32, v8
	v_bfe_i32 v10, v10, 0, 16
	v_and_b32_e32 v18, 24, v18
	v_and_b32_e32 v19, 4, v19
	v_and_or_b32 v3, v3, s6, v9
	v_or3_b32 v3, v3, v19, v18
	v_add_lshl_u32 v8, v8, v10, 1
	v_lshl_add_u32 v162, v3, 11, v8
	v_add_u32_e32 v3, 0x2000, v7
	v_ashrrev_i32_e32 v7, 31, v3
	v_lshrrev_b32_e32 v7, 22, v7
	v_add_u32_e32 v7, v3, v7
	v_ashrrev_i32_e32 v7, 10, v7
	v_mul_i32_i24_e32 v8, 0x400, v7
	v_sub_u32_e32 v3, v3, v8
	v_lshrrev_b32_e32 v8, 4, v3
	v_bitop3_b32 v3, v8, v3, 32 bitop3:0x6c
	v_ashrrev_i32_e32 v9, 31, v3
	v_lshrrev_b32_e32 v9, 26, v9
	v_add_u32_e32 v9, v3, v9
	v_lshlrev_b32_e32 v8, 3, v7
	v_ashrrev_i32_e32 v10, 6, v9
	v_and_b32_e32 v9, 0xc0, v9
	v_and_b32_e32 v8, -16, v8
	v_sub_u32_e32 v3, v3, v9
	v_add_u32_e32 v8, v10, v8
	v_lshlrev_b32_e32 v7, 5, v7
	v_ashrrev_i16_sdwa v3, v1, sext(v3) dst_sel:DWORD dst_unused:UNUSED_PAD src0_sel:DWORD src1_sel:BYTE_0
	v_and_b32_e32 v7, 32, v7
	v_bfe_i32 v3, v3, 0, 16
	v_lshlrev_b32_e32 v9, 1, v8
	v_lshrrev_b32_e32 v18, 2, v8
	v_and_b32_e32 v10, 3, v10
	v_and_b32_e32 v9, 24, v9
	v_and_b32_e32 v18, 4, v18
	v_and_or_b32 v8, v8, s6, v10
	v_add_lshl_u32 v3, v7, v3, 1
	v_mul_i32_i24_e32 v7, 64, v14
	v_or3_b32 v8, v8, v18, v9
	v_sub_u32_e32 v7, v13, v7
	v_lshl_add_u32 v164, v8, 11, v3
	v_lshlrev_b32_e32 v3, 5, v12
	v_ashrrev_i16_sdwa v7, v1, sext(v7) dst_sel:DWORD dst_unused:UNUSED_PAD src0_sel:DWORD src1_sel:BYTE_0
	v_and_b32_e32 v3, 32, v3
	v_bfe_i32 v7, v7, 0, 16
	v_add_lshl_u32 v3, v3, v7, 1
	s_waitcnt vmcnt(3)
	v_lshlrev_b32_e32 v7, 9, v15
	v_and_b32_e32 v7, 0xfffff800, v7
	v_add_u32_e32 v170, v3, v7
	s_waitcnt vmcnt(2)
	v_lshlrev_b32_e32 v7, 9, v16
	v_and_b32_e32 v7, 0xfffff800, v7
	s_add_i32 s33, s3, 0
	v_add_u32_e32 v166, v3, v7
	v_lshlrev_b32_e32 v3, 5, v4
	v_and_b32_e32 v4, 0xc0, v11
	s_add_i32 s52, s33, 0x10000
	s_add_i32 s53, s33, 0x12000
	v_sub_u32_e32 v4, v5, v4
	s_mov_b32 m0, s52
	s_add_u32 s6, s44, 0x40000
	v_ashrrev_i16_sdwa v4, v1, sext(v4) dst_sel:DWORD dst_unused:UNUSED_PAD src0_sel:DWORD src1_sel:BYTE_0
	global_load_lds_dwordx4 v162, s[44:45]
	s_mov_b32 m0, s53
	s_addc_u32 s7, s45, 0
	s_add_i32 s54, s33, 0x14000
	v_and_b32_e32 v3, 32, v3
	v_bfe_i32 v4, v4, 0, 16
	global_load_lds_dwordx4 v164, s[44:45]
	s_mov_b32 m0, s54
	s_add_i32 s55, s33, 0x16000
	v_add_lshl_u32 v3, v3, v4, 1
	s_waitcnt vmcnt(0)
	v_lshlrev_b32_e32 v4, 9, v17
	global_load_lds_dwordx4 v162, s[6:7]
	s_mov_b32 m0, s55
	s_add_u32 s22, s18, 0x4000000
	v_and_b32_e32 v4, 0xfffff800, v4
	global_load_lds_dwordx4 v164, s[6:7]
	s_addc_u32 s23, s19, 0
	s_mov_b32 m0, s33
	s_add_i32 s56, s33, 0x2000
	v_add_u32_e32 v172, v3, v4
	v_lshlrev_b32_e32 v2, 9, v2
	global_load_lds_dwordx4 v170, s[22:23]
	s_mov_b32 m0, s56
	s_add_i32 s57, s33, 0x4000
	v_and_b32_e32 v2, 0xfffff800, v2
	global_load_lds_dwordx4 v172, s[22:23]
	s_mov_b32 m0, s57
	s_add_i32 s58, s33, 0x6000
	v_add_u32_e32 v174, v3, v2
	global_load_lds_dwordx4 v166, s[22:23]
	s_mov_b32 m0, s58
	s_cmp_eq_u32 s28, 1
	global_load_lds_dwordx4 v174, s[22:23]
	v_lshl_add_u64 v[4:5], s[44:45], 0, v[162:163]
	v_lshl_add_u64 v[2:3], s[44:45], 0, v[164:165]
	s_cselect_b64 s[24:25], -1, 0
	s_cmp_lg_u32 s28, 1
	s_cbranch_scc1 .LBB0_918
	s_barrier

.LBB0_984:
	v_mov_b32_e32 v10, v0
	s_cmp_ge_i32 s90, s8
	v_readfirstlane_b32 s4, v10
	s_cbranch_scc1 .LBB0_1002
	v_bfe_i32 v3, v10, 27, 1
	v_lshlrev_b32_e32 v2, 4, v10
	v_lshrrev_b32_e32 v3, 22, v3
	v_add_u32_e32 v3, v2, v3
	v_and_b32_e32 v3, 0xfffffc00, v3
	v_sub_u32_e32 v3, v2, v3
	v_ashrrev_i32_e32 v1, 31, v10
	v_lshrrev_b32_e32 v4, 4, v3
	v_lshrrev_b32_e32 v1, 26, v1
	v_bitop3_b32 v4, v4, v3, 32 bitop3:0x6c
	v_ashrrev_i32_e32 v3, 31, v3
	v_add_u32_e32 v1, v10, v1
	v_lshrrev_b32_e32 v3, 26, v3
	v_ashrrev_i32_e32 v1, 6, v1
	v_add_u32_e32 v3, v4, v3
	v_lshlrev_b32_e32 v5, 3, v1
	v_ashrrev_i32_e32 v3, 6, v3
	v_lshlrev_b32_e32 v1, 5, v1
	v_and_b32_e32 v5, -16, v5
	v_and_b32_e32 v6, 32, v1
	v_mul_i32_i24_e32 v1, 64, v3
	v_add_u32_e32 v5, v3, v5
	v_sub_u32_e32 v4, v4, v1
	v_mov_b32_e32 v1, 1
	v_add_u32_e32 v11, 0x2000, v2
	v_ashrrev_i16_sdwa v4, v1, sext(v4) dst_sel:DWORD dst_unused:UNUSED_PAD src0_sel:DWORD src1_sel:BYTE_0
	v_lshlrev_b32_e32 v7, 1, v5
	v_lshlrev_b32_e32 v8, 2, v5
	v_lshrrev_b32_e32 v5, 2, v5
	v_and_b32_e32 v3, 3, v3
	v_ashrrev_i32_e32 v2, 31, v11
	v_bfe_i32 v4, v4, 0, 16
	v_and_b32_e32 v7, 0x1fffc0, v7
	v_and_b32_e32 v5, 4, v5
	v_and_or_b32 v3, v8, 48, v3
	v_lshrrev_b32_e32 v2, 22, v2
	v_or3_b32 v3, v3, v7, v5
	v_add_lshl_u32 v4, v6, v4, 1
	v_add_u32_e32 v2, v11, v2
	v_mov_b32_e32 v163, 0
	v_lshl_add_u32 v162, v3, 11, v4
	v_ashrrev_i32_e32 v12, 10, v2
	v_mov_b32_e32 v182, 0x20800
	ds_read_b128 v[2:5], v182 offset:16
	ds_read_b128 v[6:9], v182
	v_mul_i32_i24_e32 v13, 0x400, v12
	v_sub_u32_e32 v11, v11, v13
	v_lshrrev_b32_e32 v13, 4, v11
	v_bitop3_b32 v11, v13, v11, 32 bitop3:0x6c
	v_ashrrev_i32_e32 v14, 31, v11
	v_lshrrev_b32_e32 v14, 26, v14
	v_lshlrev_b32_e32 v13, 3, v12
	v_add_u32_e32 v14, v11, v14
	v_and_b32_e32 v13, -16, v13
	v_ashrrev_i32_e32 v15, 6, v14
	v_and_b32_e32 v14, 0xc0, v14
	v_add_u32_e32 v13, v15, v13
	v_sub_u32_e32 v11, v11, v14
	v_lshlrev_b32_e32 v12, 5, v12
	v_ashrrev_i16_sdwa v11, v1, sext(v11) dst_sel:DWORD dst_unused:UNUSED_PAD src0_sel:DWORD src1_sel:BYTE_0
	v_lshlrev_b32_e32 v14, 1, v13
	v_lshlrev_b32_e32 v16, 2, v13
	v_lshrrev_b32_e32 v13, 2, v13
	v_and_b32_e32 v15, 3, v15
	v_and_b32_e32 v12, 32, v12
	v_bfe_i32 v11, v11, 0, 16
	v_and_b32_e32 v14, 0x1fffc0, v14
	v_and_b32_e32 v13, 4, v13
	v_and_or_b32 v15, v16, 48, v15
	v_or3_b32 v13, v15, v14, v13
	v_add_lshl_u32 v11, v12, v11, 1
	v_lshl_add_u32 v164, v13, 11, v11
	ds_read_b128 v[12:15], v182 offset:48
	ds_read_b128 v[16:19], v182 offset:32
	s_ashr_i32 s1, s90, 31
	s_lshr_b32 s2, s1, 29
	s_add_i32 s2, s90, s2
	s_ashr_i32 s3, s2, 3
	s_and_b32 s2, s2, -8
	s_sub_i32 s2, s90, s2
	s_lshr_b32 s6, s2, 31
	s_add_i32 s6, s0, s6
	s_mul_i32 s2, s6, s2
	s_add_i32 s3, s2, s3
	s_ashr_i32 s2, s3, 31
	s_lshr_b32 s2, s2, 27
	s_add_i32 s6, s3, s2
	s_ashr_i32 s2, s6, 5
	s_lshl_b32 s7, s2, 2
	s_sub_i32 s2, s0, s7
	s_min_i32 s11, s2, 4
	s_abs_i32 s18, s11
	v_cvt_f32_u32_e32 v11, s18
	s_sub_i32 s20, 0, s18
	s_andn2_b32 s6, s6, 31
	s_sub_i32 s3, s3, s6
	v_rcp_iflag_f32_e32 v11, v11
	s_abs_i32 s19, s3
	s_ashr_i32 s10, s4, 6
	s_xor_b32 s6, s3, s11
	v_mul_f32_e32 v11, 0x4f7ffffe, v11
	v_cvt_u32_f32_e32 v11, v11
	s_ashr_i32 s5, s4, 8
	s_lshl_b32 s2, s10, 10
	s_ashr_i32 s6, s6, 31
	v_readfirstlane_b32 s21, v11
	s_mul_i32 s20, s20, s21
	s_mul_hi_u32 s20, s21, s20
	s_add_i32 s21, s21, s20
	s_mul_hi_u32 s20, s19, s21
	s_mul_i32 s21, s20, s18
	s_sub_i32 s19, s19, s21
	s_add_i32 s21, s20, 1
	s_sub_i32 s22, s19, s18
	s_cmp_ge_u32 s19, s18
	s_cselect_b32 s20, s21, s20
	s_cselect_b32 s19, s22, s19
	s_add_i32 s21, s20, 1
	s_cmp_ge_u32 s19, s18
	s_cselect_b32 s18, s21, s20
	s_xor_b32 s18, s18, s6
	s_sub_i32 s24, s18, s6
	s_mul_i32 s6, s24, s11
	s_sub_i32 s3, s3, s6
	s_add_i32 s18, s3, s7
	s_waitcnt lgkmcnt(2)
	v_add_u32_e32 v6, 0xff, v6
	v_add_u32_e32 v7, 0xff, v7
	v_ashrrev_i32_e32 v7, 8, v7
	v_ashrrev_i32_e32 v6, 8, v6
	v_cmp_ge_i32_e32 vcc, s18, v6
	v_add_u32_e32 v6, v7, v6
	v_add_u32_e32 v8, 0xff, v8
	v_cmp_lt_i32_e64 s[6:7], s18, v6
	v_ashrrev_i32_e32 v8, 8, v8
	s_and_b64 s[6:7], vcc, s[6:7]
	v_cmp_ge_i32_e32 vcc, s18, v6
	v_add_u32_e32 v6, v8, v6
	v_add_u32_e32 v8, 0xff, v9
	v_cndmask_b32_e64 v7, 0, 1, s[6:7]
	v_cmp_lt_i32_e64 s[6:7], s18, v6
	v_ashrrev_i32_e32 v8, 8, v8
	s_and_b64 s[6:7], vcc, s[6:7]
	v_cmp_ge_i32_e32 vcc, s18, v6
	v_add_u32_e32 v6, v8, v6
	v_add_u32_e32 v2, 0xff, v2
	v_cndmask_b32_e64 v7, v7, 2, s[6:7]
	v_cmp_lt_i32_e64 s[6:7], s18, v6
	v_ashrrev_i32_e32 v2, 8, v2
	s_and_b64 s[6:7], vcc, s[6:7]
	v_add_u32_e32 v2, v2, v6
	v_add_u32_e32 v3, 0xff, v3
	v_cndmask_b32_e64 v7, v7, 3, s[6:7]
	v_cmp_ge_i32_e32 vcc, s18, v6
	v_cmp_lt_i32_e64 s[6:7], s18, v2
	v_ashrrev_i32_e32 v3, 8, v3
	s_and_b64 s[6:7], vcc, s[6:7]
	v_cmp_ge_i32_e32 vcc, s18, v2
	v_add_u32_e32 v2, v3, v2
	v_add_u32_e32 v4, 0xff, v4
	v_cndmask_b32_e64 v11, v7, 4, s[6:7]
	ds_read_b128 v[6:9], v182 offset:80
	ds_read_b128 v[20:23], v182 offset:64
	v_cmp_lt_i32_e64 s[6:7], s18, v2
	v_ashrrev_i32_e32 v4, 8, v4
	s_and_b64 s[6:7], vcc, s[6:7]
	v_cmp_ge_i32_e32 vcc, s18, v2
	v_add_u32_e32 v2, v4, v2
	v_add_u32_e32 v4, 0xff, v5
	v_cndmask_b32_e64 v3, v11, 5, s[6:7]
	v_cmp_lt_i32_e64 s[6:7], s18, v2
	v_ashrrev_i32_e32 v4, 8, v4
	s_and_b64 s[6:7], vcc, s[6:7]
	v_cmp_ge_i32_e32 vcc, s18, v2
	v_add_u32_e32 v2, v4, v2
	s_waitcnt lgkmcnt(2)
	v_add_u32_e32 v4, 0xff, v16
	v_cndmask_b32_e64 v3, v3, 6, s[6:7]
	v_cmp_lt_i32_e64 s[6:7], s18, v2
	v_ashrrev_i32_e32 v4, 8, v4
	s_and_b64 s[6:7], vcc, s[6:7]
	v_cmp_ge_i32_e32 vcc, s18, v2
	v_add_u32_e32 v2, v4, v2
	v_add_u32_e32 v4, 0xff, v17
	v_cndmask_b32_e64 v3, v3, 7, s[6:7]
	v_cmp_lt_i32_e64 s[6:7], s18, v2
	v_ashrrev_i32_e32 v4, 8, v4
	s_and_b64 s[6:7], vcc, s[6:7]
	v_cmp_ge_i32_e32 vcc, s18, v2
	v_add_u32_e32 v2, v4, v2
	v_add_u32_e32 v4, 0xff, v18
	v_cndmask_b32_e64 v3, v3, 8, s[6:7]
	v_cmp_lt_i32_e64 s[6:7], s18, v2
	v_ashrrev_i32_e32 v4, 8, v4
	s_and_b64 s[6:7], vcc, s[6:7]
	v_cmp_ge_i32_e32 vcc, s18, v2
	v_add_u32_e32 v2, v4, v2
	v_add_u32_e32 v4, 0xff, v19
	v_cndmask_b32_e64 v3, v3, 9, s[6:7]
	v_cmp_lt_i32_e64 s[6:7], s18, v2
	v_ashrrev_i32_e32 v4, 8, v4
	s_and_b64 s[6:7], vcc, s[6:7]
	v_cmp_ge_i32_e32 vcc, s18, v2
	v_add_u32_e32 v2, v4, v2
	v_cndmask_b32_e64 v3, v3, 10, s[6:7]
	v_cmp_lt_i32_e64 s[6:7], s18, v2
	s_and_b64 s[6:7], vcc, s[6:7]
	v_cmp_ge_i32_e32 vcc, s18, v2
	v_cndmask_b32_e64 v11, v3, 11, s[6:7]
	v_add_u32_e32 v3, 0xff, v12
	v_ashrrev_i32_e32 v3, 8, v3
	v_add_u32_e32 v12, v3, v2
	ds_read_b128 v[2:5], v182 offset:112
	ds_read_b128 v[16:19], v182 offset:96
	v_add_u32_e32 v13, 0xff, v13
	v_cmp_lt_i32_e64 s[6:7], s18, v12
	v_ashrrev_i32_e32 v13, 8, v13
	s_and_b64 s[6:7], vcc, s[6:7]
	v_cmp_ge_i32_e32 vcc, s18, v12
	v_add_u32_e32 v12, v13, v12
	v_add_u32_e32 v13, 0xff, v14
	v_cndmask_b32_e64 v11, v11, 12, s[6:7]
	v_cmp_lt_i32_e64 s[6:7], s18, v12
	v_ashrrev_i32_e32 v13, 8, v13
	s_and_b64 s[6:7], vcc, s[6:7]
	v_cmp_ge_i32_e32 vcc, s18, v12
	v_add_u32_e32 v12, v13, v12
	v_add_u32_e32 v13, 0xff, v15
	v_cndmask_b32_e64 v11, v11, 13, s[6:7]
	v_cmp_lt_i32_e64 s[6:7], s18, v12
	v_ashrrev_i32_e32 v13, 8, v13
	s_and_b64 s[6:7], vcc, s[6:7]
	v_cmp_ge_i32_e32 vcc, s18, v12
	v_add_u32_e32 v12, v13, v12
	v_cndmask_b32_e64 v11, v11, 14, s[6:7]
	v_cmp_lt_i32_e64 s[6:7], s18, v12
	s_and_b64 s[6:7], vcc, s[6:7]
	v_cmp_ge_i32_e32 vcc, s18, v12
	v_cndmask_b32_e64 v11, v11, 15, s[6:7]
	s_ashr_i32 s19, s18, 31
	v_mov_b32_e32 v165, v163
	v_mov_b32_e32 v167, v163
	v_mov_b32_e32 v171, v163
	s_waitcnt lgkmcnt(3)
	v_add_u32_e32 v6, 0xff, v6
	s_waitcnt lgkmcnt(2)
	v_add_u32_e32 v13, 0xff, v20
	v_ashrrev_i32_e32 v13, 8, v13
	v_add_u32_e32 v12, v13, v12
	v_add_u32_e32 v13, 0xff, v21
	v_cmp_lt_i32_e64 s[6:7], s18, v12
	v_ashrrev_i32_e32 v13, 8, v13
	s_and_b64 s[6:7], vcc, s[6:7]
	v_cmp_ge_i32_e32 vcc, s18, v12
	v_add_u32_e32 v12, v13, v12
	v_add_u32_e32 v13, 0xff, v22
	v_cndmask_b32_e64 v11, v11, 16, s[6:7]
	v_cmp_lt_i32_e64 s[6:7], s18, v12
	v_ashrrev_i32_e32 v13, 8, v13
	s_and_b64 s[6:7], vcc, s[6:7]
	v_cmp_ge_i32_e32 vcc, s18, v12
	v_add_u32_e32 v12, v13, v12
	v_add_u32_e32 v13, 0xff, v23
	v_cndmask_b32_e64 v11, v11, 17, s[6:7]
	v_cmp_lt_i32_e64 s[6:7], s18, v12
	v_ashrrev_i32_e32 v13, 8, v13
	s_and_b64 s[6:7], vcc, s[6:7]
	v_cmp_ge_i32_e32 vcc, s18, v12
	v_add_u32_e32 v12, v13, v12
	v_cndmask_b32_e64 v11, v11, 18, s[6:7]
	v_cmp_lt_i32_e64 s[6:7], s18, v12
	v_ashrrev_i32_e32 v6, 8, v6
	s_and_b64 s[6:7], vcc, s[6:7]
	v_add_u32_e32 v6, v6, v12
	v_add_u32_e32 v7, 0xff, v7
	v_cndmask_b32_e64 v11, v11, 19, s[6:7]
	v_cmp_ge_i32_e32 vcc, s18, v12
	v_cmp_lt_i32_e64 s[6:7], s18, v6
	v_ashrrev_i32_e32 v7, 8, v7
	s_and_b64 s[6:7], vcc, s[6:7]
	v_cmp_ge_i32_e32 vcc, s18, v6
	v_add_u32_e32 v6, v7, v6
	v_add_u32_e32 v8, 0xff, v8
	v_cndmask_b32_e64 v11, v11, 20, s[6:7]
	v_cmp_lt_i32_e64 s[6:7], s18, v6
	v_ashrrev_i32_e32 v8, 8, v8
	s_and_b64 s[6:7], vcc, s[6:7]
	v_cmp_ge_i32_e32 vcc, s18, v6
	v_add_u32_e32 v6, v8, v6
	v_add_u32_e32 v8, 0xff, v9
	v_cndmask_b32_e64 v7, v11, 21, s[6:7]
	v_cmp_lt_i32_e64 s[6:7], s18, v6
	v_ashrrev_i32_e32 v8, 8, v8
	s_and_b64 s[6:7], vcc, s[6:7]
	v_cmp_ge_i32_e32 vcc, s18, v6
	v_add_u32_e32 v6, v8, v6
	s_waitcnt lgkmcnt(0)
	v_add_u32_e32 v8, 0xff, v16
	v_cndmask_b32_e64 v7, v7, 22, s[6:7]
	v_cmp_lt_i32_e64 s[6:7], s18, v6
	v_ashrrev_i32_e32 v8, 8, v8
	s_and_b64 s[6:7], vcc, s[6:7]
	v_cmp_ge_i32_e32 vcc, s18, v6
	v_add_u32_e32 v6, v8, v6
	v_add_u32_e32 v8, 0xff, v17
	v_cndmask_b32_e64 v7, v7, 23, s[6:7]
	v_cmp_lt_i32_e64 s[6:7], s18, v6
	v_ashrrev_i32_e32 v8, 8, v8
	s_and_b64 s[6:7], vcc, s[6:7]
	v_cmp_ge_i32_e32 vcc, s18, v6
	v_add_u32_e32 v6, v8, v6
	v_add_u32_e32 v8, 0xff, v18
	v_cndmask_b32_e64 v7, v7, 24, s[6:7]
	v_cmp_lt_i32_e64 s[6:7], s18, v6
	v_ashrrev_i32_e32 v8, 8, v8
	s_and_b64 s[6:7], vcc, s[6:7]
	v_cmp_ge_i32_e32 vcc, s18, v6
	v_add_u32_e32 v6, v8, v6
	v_add_u32_e32 v8, 0xff, v19
	v_cndmask_b32_e64 v7, v7, 25, s[6:7]
	v_cmp_lt_i32_e64 s[6:7], s18, v6
	v_ashrrev_i32_e32 v8, 8, v8
	s_and_b64 s[6:7], vcc, s[6:7]
	v_cmp_ge_i32_e32 vcc, s18, v6
	v_add_u32_e32 v6, v8, v6
	v_add_u32_e32 v2, 0xff, v2
	v_cndmask_b32_e64 v7, v7, 26, s[6:7]
	v_cmp_lt_i32_e64 s[6:7], s18, v6
	v_ashrrev_i32_e32 v2, 8, v2
	s_and_b64 s[6:7], vcc, s[6:7]
	v_add_u32_e32 v2, v2, v6
	v_add_u32_e32 v3, 0xff, v3
	v_cndmask_b32_e64 v7, v7, 27, s[6:7]
	v_cmp_ge_i32_e32 vcc, s18, v6
	v_cmp_lt_i32_e64 s[6:7], s18, v2
	v_ashrrev_i32_e32 v3, 8, v3
	s_and_b64 s[6:7], vcc, s[6:7]
	v_cmp_ge_i32_e32 vcc, s18, v2
	v_add_u32_e32 v2, v3, v2
	v_add_u32_e32 v4, 0xff, v4
	v_cndmask_b32_e64 v6, v7, 28, s[6:7]
	v_cmp_lt_i32_e64 s[6:7], s18, v2
	v_ashrrev_i32_e32 v4, 8, v4
	s_and_b64 s[6:7], vcc, s[6:7]
	v_cmp_ge_i32_e32 vcc, s18, v2
	v_add_u32_e32 v2, v4, v2
	v_add_u32_e32 v4, 0xff, v5
	v_cndmask_b32_e64 v3, v6, 29, s[6:7]
	v_cmp_lt_i32_e64 s[6:7], s18, v2
	v_ashrrev_i32_e32 v4, 8, v4
	s_and_b64 s[6:7], vcc, s[6:7]
	v_cmp_ge_i32_e32 vcc, s18, v2
	v_add_u32_e32 v2, v4, v2
	v_cndmask_b32_e64 v3, v3, 30, s[6:7]
	v_cmp_lt_i32_e64 s[6:7], s18, v2
	s_and_b64 s[6:7], vcc, s[6:7]
	s_mov_b32 s54, 0
	v_cndmask_b32_e64 v2, v3, 31, s[6:7]
	s_lshl_b64 s[6:7], s[18:19], 19
	v_readfirstlane_b32 s36, v2
	v_mov_b32_e32 v2, v0
	s_add_u32 s3, s14, 0x7e000000
	v_ashrrev_i32_e32 v4, 31, v2
	v_lshrrev_b32_e32 v4, 26, v4
	v_lshlrev_b32_e32 v3, 4, v2
	v_add_u32_e32 v4, v2, v4
	v_bfe_i32 v2, v2, 27, 1
	v_lshrrev_b32_e32 v2, 22, v2
	v_add_u32_e32 v2, v3, v2
	v_and_b32_e32 v2, 0xfffffc00, v2
	v_sub_u32_e32 v2, v3, v2
	v_lshrrev_b32_e32 v5, 4, v2
	v_bitop3_b32 v5, v5, v2, 32 bitop3:0x6c
	v_ashrrev_i32_e32 v2, 31, v2
	v_lshrrev_b32_e32 v2, 26, v2
	v_add_u32_e32 v2, v5, v2
	v_ashrrev_i32_e32 v2, 6, v2
	v_ashrrev_i32_e32 v4, 6, v4
	v_mul_i32_i24_e32 v7, 64, v2
	v_lshlrev_b32_e32 v6, 3, v4
	v_lshlrev_b32_e32 v4, 5, v4
	v_sub_u32_e32 v5, v5, v7
	v_and_b32_e32 v6, 0x1ffff0, v6
	v_and_b32_e32 v4, 32, v4
	v_ashrrev_i16_sdwa v5, v1, sext(v5) dst_sel:DWORD dst_unused:UNUSED_PAD src0_sel:DWORD src1_sel:BYTE_0
	v_add_u32_sdwa v4, v4, sext(v5) dst_sel:DWORD dst_unused:UNUSED_PAD src0_sel:DWORD src1_sel:WORD_0
	v_add_lshl_u32 v2, v2, v6, 11
	v_lshl_add_u32 v166, v4, 1, v2
	v_add_u32_e32 v2, 0x2000, v3
	v_ashrrev_i32_e32 v3, 31, v2
	s_addc_u32 s19, s15, 0
	s_ashr_i32 s37, s36, 31
	s_ashr_i32 s25, s24, 31
	v_lshrrev_b32_e32 v3, 22, v3
	s_lshl_b64 s[20:21], s[24:25], 19
	s_lshl_b64 s[22:23], s[36:37], 22
	v_add_u32_e32 v3, v2, v3
	s_add_u32 s11, s3, s22
	v_ashrrev_i32_e32 v3, 10, v3
	s_addc_u32 s22, s19, s23
	v_mul_i32_i24_e32 v4, 0x400, v3
	s_add_u32 s42, s11, s20
	v_sub_u32_e32 v2, v2, v4
	s_addc_u32 s43, s22, s21
	v_lshrrev_b32_e32 v4, 4, v2
	s_add_i32 s25, s2, 0
	v_bitop3_b32 v2, v4, v2, 32 bitop3:0x6c
	s_add_i32 s33, s25, 0x10000
	s_add_i32 s46, s25, 0x12000
	v_ashrrev_i32_e32 v5, 31, v2
	s_add_u32 s47, s14, 0x3a000000
	v_lshrrev_b32_e32 v5, 26, v5
	s_addc_u32 s48, s15, 0
	v_add_u32_e32 v5, v2, v5
	s_mov_b32 m0, s33
	s_add_u32 s20, s42, 0x4000
	v_lshrrev_b32_e32 v6, 6, v5
	v_and_b32_e32 v5, 0xc0, v5
	global_load_lds_dwordx4 v162, s[42:43]
	s_mov_b32 m0, s46
	s_addc_u32 s21, s43, 0
	s_add_i32 s49, s25, 0x14000
	v_lshlrev_b32_e32 v4, 3, v3
	v_lshlrev_b32_e32 v3, 5, v3
	v_sub_u32_e32 v2, v2, v5
	global_load_lds_dwordx4 v164, s[42:43]
	s_mov_b32 m0, s49
	s_add_i32 s50, s25, 0x16000
	v_and_b32_e32 v4, 0x1ffff0, v4
	v_and_b32_e32 v3, 32, v3
	v_ashrrev_i16_sdwa v2, v1, sext(v2) dst_sel:DWORD dst_unused:UNUSED_PAD src0_sel:DWORD src1_sel:BYTE_0
	global_load_lds_dwordx4 v162, s[20:21]
	s_mov_b32 m0, s50
	s_add_u32 s40, s47, s6
	v_add_u32_sdwa v2, v3, sext(v2) dst_sel:DWORD dst_unused:UNUSED_PAD src0_sel:DWORD src1_sel:WORD_0
	v_add_lshl_u32 v3, v6, v4, 11
	global_load_lds_dwordx4 v164, s[20:21]
	s_addc_u32 s41, s48, s7
	s_mov_b32 m0, s25
	s_add_i32 s51, s25, 0x2000
	v_lshl_add_u32 v170, v2, 1, v3
	global_load_lds_dwordx4 v166, s[40:41]
	s_mov_b32 m0, s51
	s_add_i32 s52, s25, 0x4000
	v_add_u32_e32 v168, 0x40000, v166
	global_load_lds_dwordx4 v170, s[40:41]
	s_mov_b32 m0, s52
	s_add_i32 s53, s25, 0x6000
	v_add_u32_e32 v172, 0x40000, v170
	global_load_lds_dwordx4 v168, s[40:41]
	s_mov_b32 m0, s53
	s_cmp_eq_u32 s5, 1
	global_load_lds_dwordx4 v172, s[40:41]
	s_mov_b32 s55, 0x40000
	v_lshl_add_u64 v[8:9], s[42:43], 0, v[162:163]
	v_lshl_add_u64 v[6:7], s[42:43], 0, v[164:165]
	v_lshl_add_u64 v[2:3], s[40:41], 0, v[166:167]
	s_cselect_b64 s[20:21], -1, 0
	s_cmp_lg_u32 s5, 1
	v_lshl_add_u64 v[4:5], s[40:41], 0, v[170:171]
	s_cbranch_scc1 .LBB0_987
	s_barrier
